# MLA leading-half unit epilogue: 16 partner partial-O LDS reads issued 8/4/4 with counted lgkmcnt instead of one read per lgkmcnt(0); on top of earlier de-serialisation edits (MLA loop reorder, out-pro
# baseline (speedup 1.0000x reference)
; #define LAS __attribute__((address_space(3)))
; __device__ __forceinline__ unsigned cvtpk(float lo, float hi) { f32x2 v = {lo, hi}; bf16x2_t b = __builtin_convertvector(v, bf16x2_t); return __builtin_bit_cast(unsigned, b); }
; #define ATT_SB() __builtin_amdgcn_sched_barrier(0)
; #define ATT_VLOAD(sl, h_) do { _Pragma("unroll") for (int g_ = 0; g_ < NVF; ++g_) { \
;         if constexpr (KS) vf[g_] = *(const LAS bf16x8*)(vpk + (sl) * VSLOT + g_ * 2048); \
;         else vf[g_] = *(const LAS bf16x8*)(vp[g_ & 1] + (sl) * VSLOT + ((h_) * 4 + (g_ >> 1)) * 2048); } } while (0)
; template <int DQK, int DV, bool LEAD> ...
;     ...
;     ATT_VLOAD(s_prev, 0); ATT_PVP(0);
;     if constexpr (DV == 128) { ATT_SB(); ATT_VLOAD(s_prev, 1); ATT_PVP(1); }
; #pragma unroll
;     for (int qb = 0; qb < NQB; ++qb) lsum[qb] = lanes4_sum(lsum[qb]);
;     if constexpr (KS) {
;         wait_bar<0>();
;         LAS unsigned char* xch = shm + (wid & 3) * 17408;
;         if constexpr (!LEAD) {
; #pragma unroll
;             for (int db = 0; db < 4; ++db)
; #pragma unroll
;                 for (int qb = 0; qb < 4; ++qb) *(LAS f32x4*)(xch + ((db * 4 + qb) * 64 + lane) * 16) = o[db][qb];
; #pragma unroll
;             for (int qb = 0; qb < 4; ++qb) *(LAS float*)(xch + 16384 + (qb * 64 + lane) * 4) = lsum[qb];
;         }
;         asm volatile("s_waitcnt lgkmcnt(0)\n\ts_barrier" ::: "memory");
;         if constexpr (LEAD) {
;             float inv[4];
; #pragma unroll
;             for (int qb = 0; qb < 4; ++qb) inv[qb] = 1.0f / (lsum[qb] + *(const LAS float*)(xch + 16384 + (qb * 64 + lane) * 4));
;             LAS unsigned char* stg = shm + ATT_LDS + (wid & 3) * 8192;
; #pragma unroll
;             for (int dbl = 0; dbl < 4; ++dbl)
; #pragma unroll
;                 for (int qb = 0; qb < 4; ++qb) { const f32x4 ov = o[dbl][qb] + *(const LAS f32x4*)(xch + ((dbl * 4 + qb) * 64 + lane) * 16); const int row = qb * 16 + q16;
;                     u32x2 w; w.x = cvtpk(ov[0] * inv[qb], ov[1] * inv[qb]); w.y = cvtpk(ov[2] * inv[qb], ov[3] * inv[qb]);
;                     *(LAS u32x2*)(stg + row * 128 + (((4 * dbl + g4) ^ ((row & 7) << 1)) << 3)) = w; }
.LBB0_639:
	v_lshl_add_u32 v14, s31, 13, v210
	ds_read_b128 v[2:5], v14 offset:36864
	ds_read_b128 v[6:9], v14 offset:38912
	ds_read_b128 v[10:13], v14 offset:40960
	s_waitcnt lgkmcnt(4)
	ds_read_b128 v[66:69], v14 offset:43008
	s_lshl_b32 s4, s6, 1
	s_waitcnt lgkmcnt(3)
	v_mfma_f32_16x16x32_bf16 v[62:65], v[2:5], v[138:141], v[134:137]
	s_add_u32 s4, s14, s4
	s_mul_i32 s6, s30, 0x4400
	s_addc_u32 s5, s15, 0
	v_mfma_f32_16x16x32_bf16 v[58:61], v[2:5], v[142:145], v[130:133]
	s_waitcnt vmcnt(0) lgkmcnt(0)
	s_barrier
	s_add_i32 s7, s6, 0
	s_waitcnt lgkmcnt(0)
	s_barrier
	v_mfma_f32_16x16x32_bf16 v[54:57], v[2:5], v[146:149], v[126:129]
	v_lshl_add_u32 v70, v218, 2, s7
	s_lshl_b32 s6, s30, 13
	s_add_i32 s6, s6, 0
	v_mfma_f32_16x16x32_bf16 v[50:53], v[2:5], v[150:153], v[122:125]
	s_add_i32 s6, s6, 0x15000
	s_waitcnt lgkmcnt(2)
	v_mfma_f32_16x16x32_bf16 v[46:49], v[6:9], v[138:141], v[118:121]
	v_mfma_f32_16x16x32_bf16 v[42:45], v[6:9], v[142:145], v[114:117]
	v_mfma_f32_16x16x32_bf16 v[38:41], v[6:9], v[146:149], v[110:113]
	v_mfma_f32_16x16x32_bf16 v[34:37], v[6:9], v[150:153], v[106:109]
	s_waitcnt lgkmcnt(1)
	v_mfma_f32_16x16x32_bf16 v[30:33], v[10:13], v[138:141], v[102:105]
	v_mfma_f32_16x16x32_bf16 v[26:29], v[10:13], v[142:145], v[98:101]
	v_mfma_f32_16x16x32_bf16 v[22:25], v[10:13], v[146:149], v[94:97]
	v_mfma_f32_16x16x32_bf16 v[18:21], v[10:13], v[150:153], v[90:93]
	s_waitcnt lgkmcnt(0)
	v_mfma_f32_16x16x32_bf16 v[14:17], v[66:69], v[138:141], v[86:89]
	v_mfma_f32_16x16x32_bf16 v[10:13], v[66:69], v[142:145], v[82:85]
	v_mfma_f32_16x16x32_bf16 v[6:9], v[66:69], v[146:149], v[78:81]
	v_mfma_f32_16x16x32_bf16 v[2:5], v[66:69], v[150:153], v[74:77]
	v_mov_b32_e32 v66, v205
	s_nop 1
	v_permlane16_swap_b32_e32 v205, v66
	v_add_f32_e32 v66, v205, v66
	v_mov_b32_e32 v67, v66
	s_nop 1
	v_permlane32_swap_b32_e32 v66, v67
	v_add_f32_e32 v68, v66, v67
	v_mov_b32_e32 v66, v204
	s_nop 1
	v_permlane16_swap_b32_e32 v204, v66
	v_add_f32_e32 v66, v204, v66
	v_mov_b32_e32 v67, v66
	s_nop 1
	v_permlane32_swap_b32_e32 v66, v67
	v_add_f32_e32 v69, v66, v67
	v_mov_b32_e32 v66, v193
	s_nop 1
	v_permlane16_swap_b32_e32 v193, v66
	v_add_f32_e32 v66, v193, v66
	v_mov_b32_e32 v67, v66
	s_nop 1
	v_permlane32_swap_b32_e32 v66, v67
	v_add_f32_e32 v72, v66, v67
	v_mov_b32_e32 v66, v192
	s_nop 1
	v_permlane16_swap_b32_e32 v192, v66
	v_add_f32_e32 v66, v192, v66
	v_mov_b32_e32 v67, v66
	s_nop 1
	v_permlane32_swap_b32_e32 v66, v67
	v_add_f32_e32 v73, v66, v67
	ds_read2st64_b32 v[66:67], v70 offset0:64 offset1:65
	s_waitcnt lgkmcnt(0)
	v_add_f32_e32 v66, v68, v66
	v_div_scale_f32 v68, s[40:41], v66, v66, 1.0
	v_rcp_f32_e32 v71, v68
	s_nop 0
	v_fma_f32 v74, -v68, v71, 1.0
	v_fmac_f32_e32 v71, v74, v71
	v_div_scale_f32 v74, vcc, 1.0, v66, 1.0
	v_mul_f32_e32 v75, v74, v71
	v_fma_f32 v76, -v68, v75, v74
	v_fmac_f32_e32 v75, v76, v71
	v_fma_f32 v68, -v68, v75, v74
	v_div_fmas_f32 v68, v68, v71, v75
	v_div_fixup_f32 v68, v68, v66, 1.0
	v_add_f32_e32 v66, v69, v67
	v_div_scale_f32 v67, s[40:41], v66, v66, 1.0
	v_rcp_f32_e32 v69, v67
	s_nop 0
	v_fma_f32 v71, -v67, v69, 1.0
	v_fmac_f32_e32 v69, v71, v69
	v_div_scale_f32 v71, vcc, 1.0, v66, 1.0
	v_mul_f32_e32 v74, v71, v69
	v_fma_f32 v75, -v67, v74, v71
	v_fmac_f32_e32 v74, v75, v69
	v_fma_f32 v67, -v67, v74, v71
	ds_read2st64_b32 v[70:71], v70 offset0:66 offset1:67
	v_div_fmas_f32 v67, v67, v69, v74
	v_div_fixup_f32 v66, v67, v66, 1.0
	s_waitcnt lgkmcnt(0)
	v_add_f32_e32 v67, v72, v70
	v_div_scale_f32 v69, s[40:41], v67, v67, 1.0
	v_rcp_f32_e32 v70, v69
	s_nop 0
	v_fma_f32 v72, -v69, v70, 1.0
	v_fmac_f32_e32 v70, v72, v70
	v_div_scale_f32 v72, vcc, 1.0, v67, 1.0
	v_mul_f32_e32 v74, v72, v70
	v_fma_f32 v75, -v69, v74, v72
	v_fmac_f32_e32 v74, v75, v70
	v_fma_f32 v69, -v69, v74, v72
	v_div_fmas_f32 v69, v69, v70, v74
	v_div_fixup_f32 v72, v69, v67, 1.0
	v_add_f32_e32 v67, v73, v71
	v_div_scale_f32 v69, s[40:41], v67, v67, 1.0
	v_rcp_f32_e32 v70, v69
	s_nop 0
	v_fma_f32 v71, -v69, v70, 1.0
	v_fmac_f32_e32 v70, v71, v70
	v_div_scale_f32 v71, vcc, 1.0, v67, 1.0
	v_mul_f32_e32 v73, v71, v70
	v_fma_f32 v74, -v69, v73, v71
	v_fmac_f32_e32 v73, v74, v70
	v_fma_f32 v69, -v69, v73, v71
	v_div_fmas_f32 v69, v69, v70, v73
	v_div_fixup_f32 v70, v69, v67, 1.0
	v_lshl_add_u32 v67, v218, 4, s7
	ds_read_b128 v[154:157], v67
	ds_read_b128 v[158:161], v67 offset:1024
	ds_read_b128 v[162:165], v67 offset:2048
	ds_read_b128 v[166:169], v67 offset:3072
	ds_read_b128 v[170:173], v67 offset:4096
	ds_read_b128 v[174:177], v67 offset:5120
	ds_read_b128 v[178:181], v67 offset:6144
	ds_read_b128 v[182:185], v67 offset:7168
	v_add_u32_e32 v69, s6, v207
	v_bitop3_b32 v73, v194, v217, 14 bitop3:0x78
	v_lshl_add_u32 v73, v73, 3, v69
	v_and_b32_e32 v71, 14, v217
	s_waitcnt lgkmcnt(4)
	v_pk_add_f32 v[62:63], v[62:63], v[154:155]
	v_pk_add_f32 v[64:65], v[64:65], v[156:157]
	v_pk_mul_f32 v[62:63], v[68:69], v[62:63] op_sel_hi:[0,1]
	v_cvt_pk_bf16_f32 v74, v62, v63
	v_pk_mul_f32 v[62:63], v[68:69], v[64:65] op_sel_hi:[0,1]
	v_cvt_pk_bf16_f32 v75, v62, v63
	v_pk_add_f32 v[60:61], v[60:61], v[160:161]
	v_pk_add_f32 v[58:59], v[58:59], v[158:159]
	v_pk_mul_f32 v[60:61], v[66:67], v[60:61] op_sel_hi:[0,1]
	v_pk_mul_f32 v[58:59], v[66:67], v[58:59] op_sel_hi:[0,1]
	v_cvt_pk_bf16_f32 v58, v58, v59
	v_cvt_pk_bf16_f32 v59, v60, v61
	ds_write2st64_b64 v73, v[74:75], v[58:59] offset1:4
	v_pk_add_f32 v[54:55], v[54:55], v[162:163]
	v_pk_add_f32 v[56:57], v[56:57], v[164:165]
	v_pk_mul_f32 v[54:55], v[72:73], v[54:55] op_sel_hi:[0,1]
	v_cvt_pk_bf16_f32 v58, v54, v55
	v_pk_mul_f32 v[54:55], v[72:73], v[56:57] op_sel_hi:[0,1]
	v_cvt_pk_bf16_f32 v59, v54, v55
	v_pk_add_f32 v[52:53], v[52:53], v[168:169]
	v_pk_add_f32 v[50:51], v[50:51], v[166:167]
	v_pk_mul_f32 v[52:53], v[70:71], v[52:53] op_sel_hi:[0,1]
	v_pk_mul_f32 v[50:51], v[70:71], v[50:51] op_sel_hi:[0,1]
	v_cvt_pk_bf16_f32 v50, v50, v51
	v_cvt_pk_bf16_f32 v51, v52, v53
	ds_write2st64_b64 v73, v[58:59], v[50:51] offset0:8 offset1:12
	v_bitop3_b32 v50, v206, v217, 14 bitop3:0x78
	v_lshl_add_u32 v54, v50, 3, v69
	ds_read_b128 v[154:157], v67 offset:8192
	ds_read_b128 v[158:161], v67 offset:9216
	ds_read_b128 v[162:165], v67 offset:10240
	ds_read_b128 v[166:169], v67 offset:11264
	s_waitcnt lgkmcnt(6)
; #define LAS __attribute__((address_space(3)))
; __device__ __forceinline__ unsigned cvtpk(float lo, float hi) { f32x2 v = {lo, hi}; bf16x2_t b = __builtin_convertvector(v, bf16x2_t); return __builtin_bit_cast(unsigned, b); }
; template <int DQK, int DV, bool LEAD> ...
;     ...
;             for (int qb = 0; qb < 4; ++qb) inv[qb] = 1.0f / (lsum[qb] + *(const LAS float*)(xch + 16384 + (qb * 64 + lane) * 4));
;             LAS unsigned char* stg = shm + ATT_LDS + (wid & 3) * 8192;
; #pragma unroll
;             for (int dbl = 0; dbl < 4; ++dbl)
; #pragma unroll
;                 for (int qb = 0; qb < 4; ++qb) { const f32x4 ov = o[dbl][qb] + *(const LAS f32x4*)(xch + ((dbl * 4 + qb) * 64 + lane) * 16); const int row = qb * 16 + q16;
;                     u32x2 w; w.x = cvtpk(ov[0] * inv[qb], ov[1] * inv[qb]); w.y = cvtpk(ov[2] * inv[qb], ov[3] * inv[qb]);
;                     *(LAS u32x2*)(stg + row * 128 + (((4 * dbl + g4) ^ ((row & 7) << 1)) << 3)) = w; }
;             asm volatile("s_waitcnt lgkmcnt(0)" ::: "memory");
; #pragma unroll
;             for (int rr = 0; rr < 8; ++rr) { const int row = rr * 8 + (lane >> 3), ch = lane & 7;
;                 const u32x4 v = *(const LAS u32x4*)(stg + row * 128 + ((ch ^ (row & 7)) << 4));
;                 *(u32x4*)(O + (size_t)(qrow0 + qoff + row) * opitch + ch * 8) = v; }
;             asm volatile("s_waitcnt lgkmcnt(0)" ::: "memory");
	v_pk_add_f32 v[46:47], v[46:47], v[170:171]
	v_pk_add_f32 v[48:49], v[48:49], v[172:173]
	v_pk_mul_f32 v[46:47], v[68:69], v[46:47] op_sel_hi:[0,1]
	v_cvt_pk_bf16_f32 v50, v46, v47
	v_pk_mul_f32 v[46:47], v[68:69], v[48:49] op_sel_hi:[0,1]
	v_cvt_pk_bf16_f32 v51, v46, v47
	v_pk_add_f32 v[44:45], v[44:45], v[176:177]
	v_pk_add_f32 v[42:43], v[42:43], v[174:175]
	v_pk_mul_f32 v[44:45], v[66:67], v[44:45] op_sel_hi:[0,1]
	v_pk_mul_f32 v[42:43], v[66:67], v[42:43] op_sel_hi:[0,1]
	v_cvt_pk_bf16_f32 v42, v42, v43
	v_cvt_pk_bf16_f32 v43, v44, v45
	ds_write2st64_b64 v54, v[50:51], v[42:43] offset1:4
	v_pk_add_f32 v[38:39], v[38:39], v[178:179]
	v_pk_add_f32 v[40:41], v[40:41], v[180:181]
	v_pk_mul_f32 v[38:39], v[72:73], v[38:39] op_sel_hi:[0,1]
	v_cvt_pk_bf16_f32 v42, v38, v39
	v_pk_mul_f32 v[38:39], v[72:73], v[40:41] op_sel_hi:[0,1]
	v_cvt_pk_bf16_f32 v43, v38, v39
	v_pk_add_f32 v[36:37], v[36:37], v[184:185]
	v_pk_add_f32 v[34:35], v[34:35], v[182:183]
	v_pk_mul_f32 v[36:37], v[70:71], v[36:37] op_sel_hi:[0,1]
	v_pk_mul_f32 v[34:35], v[70:71], v[34:35] op_sel_hi:[0,1]
	v_cvt_pk_bf16_f32 v34, v34, v35
	v_cvt_pk_bf16_f32 v35, v36, v37
	ds_write2st64_b64 v54, v[42:43], v[34:35] offset0:8 offset1:12
	v_bitop3_b32 v34, v194, v71, 8 bitop3:0x36
	v_lshl_add_u32 v38, v34, 3, v69
	ds_read_b128 v[170:173], v67 offset:12288
	ds_read_b128 v[174:177], v67 offset:13312
	ds_read_b128 v[178:181], v67 offset:14336
	ds_read_b128 v[182:185], v67 offset:15360
	s_waitcnt lgkmcnt(6)
	v_pk_add_f32 v[30:31], v[30:31], v[154:155]
	v_pk_add_f32 v[32:33], v[32:33], v[156:157]
	v_pk_mul_f32 v[30:31], v[68:69], v[30:31] op_sel_hi:[0,1]
	v_cvt_pk_bf16_f32 v34, v30, v31
	v_pk_mul_f32 v[30:31], v[68:69], v[32:33] op_sel_hi:[0,1]
	v_cvt_pk_bf16_f32 v35, v30, v31
	v_pk_add_f32 v[28:29], v[28:29], v[160:161]
	v_pk_add_f32 v[26:27], v[26:27], v[158:159]
	v_pk_mul_f32 v[28:29], v[66:67], v[28:29] op_sel_hi:[0,1]
	v_pk_mul_f32 v[26:27], v[66:67], v[26:27] op_sel_hi:[0,1]
	v_cvt_pk_bf16_f32 v26, v26, v27
	v_cvt_pk_bf16_f32 v27, v28, v29
	ds_write2st64_b64 v38, v[34:35], v[26:27] offset1:4
	v_pk_add_f32 v[22:23], v[22:23], v[162:163]
	v_pk_add_f32 v[24:25], v[24:25], v[164:165]
	v_pk_mul_f32 v[22:23], v[72:73], v[22:23] op_sel_hi:[0,1]
	v_cvt_pk_bf16_f32 v26, v22, v23
	v_pk_mul_f32 v[22:23], v[72:73], v[24:25] op_sel_hi:[0,1]
	v_cvt_pk_bf16_f32 v27, v22, v23
	v_pk_add_f32 v[20:21], v[20:21], v[168:169]
	v_pk_add_f32 v[18:19], v[18:19], v[166:167]
	v_pk_mul_f32 v[20:21], v[70:71], v[20:21] op_sel_hi:[0,1]
	v_pk_mul_f32 v[18:19], v[70:71], v[18:19] op_sel_hi:[0,1]
	v_cvt_pk_bf16_f32 v18, v18, v19
	v_cvt_pk_bf16_f32 v19, v20, v21
	ds_write2st64_b64 v38, v[26:27], v[18:19] offset0:8 offset1:12
	v_bitop3_b32 v18, v194, v71, 12 bitop3:0x36
	v_lshl_add_u32 v22, v18, 3, v69
	v_lshlrev_b32_e32 v194, 4, v216
	s_waitcnt lgkmcnt(2)
	v_pk_add_f32 v[14:15], v[14:15], v[170:171]
	v_pk_add_f32 v[16:17], v[16:17], v[172:173]
	v_pk_mul_f32 v[14:15], v[68:69], v[14:15] op_sel_hi:[0,1]
	v_cvt_pk_bf16_f32 v18, v14, v15
	v_pk_mul_f32 v[14:15], v[68:69], v[16:17] op_sel_hi:[0,1]
	v_cvt_pk_bf16_f32 v19, v14, v15
	v_pk_add_f32 v[12:13], v[12:13], v[176:177]
	v_pk_add_f32 v[10:11], v[10:11], v[174:175]
	v_pk_mul_f32 v[12:13], v[66:67], v[12:13] op_sel_hi:[0,1]
	v_pk_mul_f32 v[10:11], v[66:67], v[10:11] op_sel_hi:[0,1]
	v_cvt_pk_bf16_f32 v10, v10, v11
	v_cvt_pk_bf16_f32 v11, v12, v13
	ds_write2st64_b64 v22, v[18:19], v[10:11] offset1:4
	v_pk_add_f32 v[6:7], v[6:7], v[178:179]
	v_pk_add_f32 v[8:9], v[8:9], v[180:181]
	v_pk_mul_f32 v[6:7], v[72:73], v[6:7] op_sel_hi:[0,1]
	v_cvt_pk_bf16_f32 v10, v6, v7
	v_pk_mul_f32 v[6:7], v[72:73], v[8:9] op_sel_hi:[0,1]
	v_cvt_pk_bf16_f32 v11, v6, v7
	v_pk_add_f32 v[4:5], v[4:5], v[184:185]
	v_pk_add_f32 v[2:3], v[2:3], v[182:183]
	v_pk_mul_f32 v[4:5], v[70:71], v[4:5] op_sel_hi:[0,1]
	v_pk_mul_f32 v[2:3], v[70:71], v[2:3] op_sel_hi:[0,1]
	v_cvt_pk_bf16_f32 v2, v2, v3
	v_cvt_pk_bf16_f32 v3, v4, v5
	ds_write2st64_b64 v22, v[10:11], v[2:3] offset0:8 offset1:12
	v_xor_b32_e32 v2, v203, v216
	v_lshl_add_u32 v10, v2, 4, s6
	s_waitcnt lgkmcnt(0)
	v_lshl_add_u32 v2, v203, 7, v10
	ds_read_b128 v[2:5], v2
	v_or_b32_e32 v8, s25, v203
	v_ashrrev_i32_e32 v9, 31, v8
	v_lshl_add_u64 v[6:7], s[4:5], 0, v[194:195]
	v_lshlrev_b64 v[8:9], 11, v[8:9]
	v_lshl_add_u64 v[8:9], v[6:7], 0, v[8:9]
	s_waitcnt lgkmcnt(0)
	global_store_dwordx4 v[8:9], v[2:5], off
	v_or_b32_e32 v8, 8, v203
	s_nop 0
	v_lshl_add_u32 v2, v8, 7, v10
	ds_read_b128 v[2:5], v2
	v_or_b32_e32 v8, s25, v8
	v_ashrrev_i32_e32 v9, 31, v8
	v_lshlrev_b64 v[8:9], 11, v[8:9]
	v_lshl_add_u64 v[8:9], v[6:7], 0, v[8:9]
	s_waitcnt lgkmcnt(0)
	global_store_dwordx4 v[8:9], v[2:5], off
	v_or_b32_e32 v8, 16, v203
	s_nop 0
	v_lshl_add_u32 v2, v8, 7, v10
	ds_read_b128 v[2:5], v2
	v_or_b32_e32 v8, s25, v8
	v_ashrrev_i32_e32 v9, 31, v8
	v_lshlrev_b64 v[8:9], 11, v[8:9]
	v_lshl_add_u64 v[8:9], v[6:7], 0, v[8:9]
	s_waitcnt lgkmcnt(0)
	global_store_dwordx4 v[8:9], v[2:5], off
	v_or_b32_e32 v8, 24, v203
	s_nop 0
	v_lshl_add_u32 v2, v8, 7, v10
	ds_read_b128 v[2:5], v2
	v_or_b32_e32 v8, s25, v8
	v_ashrrev_i32_e32 v9, 31, v8
	v_lshlrev_b64 v[8:9], 11, v[8:9]
	v_lshl_add_u64 v[8:9], v[6:7], 0, v[8:9]
	s_waitcnt lgkmcnt(0)
	global_store_dwordx4 v[8:9], v[2:5], off
	v_or_b32_e32 v8, 32, v203
	s_nop 0
	v_lshl_add_u32 v2, v8, 7, v10
	ds_read_b128 v[2:5], v2
	v_or_b32_e32 v8, s25, v8
	v_ashrrev_i32_e32 v9, 31, v8
	v_lshlrev_b64 v[8:9], 11, v[8:9]
	v_lshl_add_u64 v[8:9], v[6:7], 0, v[8:9]
	s_waitcnt lgkmcnt(0)
	global_store_dwordx4 v[8:9], v[2:5], off
	v_or_b32_e32 v8, 40, v203
	s_nop 0
	v_lshl_add_u32 v2, v8, 7, v10
	ds_read_b128 v[2:5], v2
	v_or_b32_e32 v8, s25, v8
	v_ashrrev_i32_e32 v9, 31, v8
	v_lshlrev_b64 v[8:9], 11, v[8:9]
	v_lshl_add_u64 v[8:9], v[6:7], 0, v[8:9]
	s_waitcnt lgkmcnt(0)
	global_store_dwordx4 v[8:9], v[2:5], off
	v_or_b32_e32 v8, 48, v203
	s_nop 0
	v_lshl_add_u32 v2, v8, 7, v10
	ds_read_b128 v[2:5], v2
	v_or_b32_e32 v8, s25, v8
	v_ashrrev_i32_e32 v9, 31, v8
	v_lshlrev_b64 v[8:9], 11, v[8:9]
	v_lshl_add_u64 v[8:9], v[6:7], 0, v[8:9]
	s_waitcnt lgkmcnt(0)
	global_store_dwordx4 v[8:9], v[2:5], off
	v_or_b32_e32 v8, 56, v203
	s_nop 0
	v_lshl_add_u32 v2, v8, 7, v10
	ds_read_b128 v[2:5], v2
	v_or_b32_e32 v8, s25, v8
	v_ashrrev_i32_e32 v9, 31, v8
	v_lshlrev_b64 v[8:9], 11, v[8:9]
	v_lshl_add_u64 v[6:7], v[6:7], 0, v[8:9]
	s_waitcnt lgkmcnt(0)
	global_store_dwordx4 v[6:7], v[2:5], off
	s_waitcnt lgkmcnt(0)
	s_waitcnt lgkmcnt(0)
	s_barrier
